# v30 + tail pass reuses the LDS segment table; dtype header comment
# speedup vs baseline: 1.0007x; 1.0007x over previous
; #define LAS __attribute__((address_space(3)))
; __device__ __forceinline__ int opaque_tid() { int t = threadIdx.x; asm volatile("" : "+v"(t)); return t; }
; __device__ __forceinline__ void seg_to_lds(const Args& a, LAS unsigned char* lds, int layer) {
;     LAS int* seg = (LAS int*)(lds + SEG_OFF);
;     const int t = opaque_tid();
;     if (t < 16) {
;         unsigned* cnt = (unsigned*)(a.ws + WS_CTL) + CW_CNT + layer * 16 * 64;
;         const int c = (int)__hip_atomic_load(cnt + t * 64, __ATOMIC_RELAXED, __HIP_MEMORY_SCOPE_AGENT);
;         const int pad = (c + 255) & ~255;
;         int incl = pad;
; #pragma unroll
;         for (int o2 = 1; o2 < 16; o2 <<= 1) { const int u2 = __shfl_up(incl, o2); if (t >= o2) incl += u2; }
;         seg[t] = c; seg[16 + t] = incl - pad;
;         if (t == 15) seg[32] = incl;
;     }
;     __syncthreads();
.Lxcd_perm_skip_both:
.Lgu_restart:
	v_mov_b32_e32 v1, v0
	s_waitcnt lgkmcnt(0)
	s_barrier
	s_nop 0
	v_readlane_b32 s2, v254, 62
	s_nop 1
	s_cmp_eq_u32 s2, 1
	s_cselect_b32 s2, 0, 16
	s_nop 1
	v_cmp_gt_i32_e32 vcc, s2, v1
	s_and_saveexec_b64 s[4:5], vcc
	s_cbranch_execz .LBB0_901
	v_lshlrev_b32_e32 v2, 6, v1
	v_readlane_b32 s6, v254, 22
	v_ashrrev_i32_e32 v3, 31, v2
	v_readlane_b32 s7, v254, 23
	v_cmp_lt_i32_e32 vcc, v235, v240
	s_nop 0
	v_lshl_add_u64 v[2:3], v[2:3], 2, s[6:7]
	global_load_dword v3, v[2:3], off sc1
	s_waitcnt vmcnt(0)
	v_add_u32_e32 v2, 0xff, v3
	v_and_b32_e32 v4, 0xffffff00, v2
	v_cndmask_b32_e32 v2, v235, v199, vcc
	v_lshlrev_b32_e32 v2, 2, v2
	ds_bpermute_b32 v2, v2, v4
	v_cmp_lt_i32_e32 vcc, 0, v1
	s_waitcnt lgkmcnt(0)
	s_nop 0
	v_cndmask_b32_e32 v2, 0, v2, vcc
	v_cmp_lt_i32_e32 vcc, v233, v240
	v_add_u32_e32 v2, v4, v2
	s_nop 0
	v_cndmask_b32_e32 v5, v233, v199, vcc
	v_lshlrev_b32_e32 v5, 2, v5
	ds_bpermute_b32 v5, v5, v2
	v_cmp_lt_i32_e32 vcc, 1, v1
	s_waitcnt lgkmcnt(0)
	s_nop 0
	v_cndmask_b32_e32 v5, 0, v5, vcc
	v_cmp_lt_i32_e32 vcc, v243, v240
	v_add_u32_e32 v2, v2, v5
	s_nop 0
	v_cndmask_b32_e32 v5, v243, v199, vcc
	v_lshlrev_b32_e32 v5, 2, v5
	ds_bpermute_b32 v5, v5, v2
	v_cmp_lt_i32_e32 vcc, 3, v1
	s_waitcnt lgkmcnt(0)
	s_nop 0
	v_cndmask_b32_e32 v5, 0, v5, vcc
	v_cmp_lt_i32_e32 vcc, v203, v240
	v_add_u32_e32 v2, v2, v5
	s_nop 0
	v_cndmask_b32_e32 v5, v203, v199, vcc
	v_lshlrev_b32_e32 v5, 2, v5
	ds_bpermute_b32 v5, v5, v2
	v_cmp_lt_i32_e32 vcc, 7, v1
	s_waitcnt lgkmcnt(0)
	s_nop 0
	v_cndmask_b32_e32 v5, 0, v5, vcc
	v_add_u32_e32 v2, v2, v5
	v_lshl_add_u32 v5, v1, 2, 0
	v_add_u32_e32 v5, 0x21e00, v5
	v_sub_u32_e32 v4, v2, v4
	v_cmp_eq_u32_e32 vcc, 15, v1
	ds_write2_b32 v5, v3, v4 offset1:16
	s_and_b64 exec, exec, vcc
	s_cbranch_execz .LBB0_901
	v_readlane_b32 s2, v253, 58
	s_nop 1
	v_mov_b32_e32 v1, s2
	ds_write_b32 v1, v2
